# pool_main: the 16 pointwise-weight fragment loads moved to the start of pool_sums into conv-scratch registers, MFMAs read those (were loaded and waited inside the MFMA chain)
# baseline (speedup 1.0000x reference)
.LBB0_583:
	s_or_b64 exec, exec, s[8:9]
	s_waitcnt lgkmcnt(0)
	s_barrier
	s_load_dwordx2 s[100:101], s[0:1], 0xd0
	v_and_b32_e32 v232, 31, v234
	v_or_b32_e32 v232, s67, v232
	v_mov_b32_e32 v233, 0
	v_lshlrev_b64 v[232:233], 8, v[232:233]
	v_lshrrev_b32_e32 v248, 5, v234
	v_and_b32_e32 v248, 1, v248
	v_lshlrev_b32_e32 v248, 4, v248
	v_mov_b32_e32 v249, 0
	v_lshl_add_u64 v[232:233], v[232:233], 0, v[248:249]
	s_waitcnt lgkmcnt(0)
	v_lshl_add_u64 v[232:233], s[100:101], 0, v[232:233]
	s_mov_b32 s100, 0x1600000
	s_mov_b32 s101, 0
	v_lshl_add_u64 v[248:249], v[232:233], 0, s[100:101]
	s_mov_b32 s100, 0x1602000
	v_lshl_add_u64 v[250:251], v[232:233], 0, s[100:101]
	global_load_dwordx4 v[168:171], v[248:249], off
	global_load_dwordx4 v[172:175], v[250:251], off
	global_load_dwordx4 v[176:179], v[248:249], off offset:32
	global_load_dwordx4 v[180:183], v[250:251], off offset:32
	global_load_dwordx4 v[184:187], v[248:249], off offset:64
	global_load_dwordx4 v[188:191], v[250:251], off offset:64
	global_load_dwordx4 v[192:195], v[248:249], off offset:96
	global_load_dwordx4 v[196:199], v[250:251], off offset:96
	global_load_dwordx4 v[200:203], v[248:249], off offset:128
	global_load_dwordx4 v[204:207], v[250:251], off offset:128
	global_load_dwordx4 v[208:211], v[248:249], off offset:160
	global_load_dwordx4 v[212:215], v[250:251], off offset:160
	global_load_dwordx4 v[216:219], v[248:249], off offset:192
	global_load_dwordx4 v[220:223], v[250:251], off offset:192
	global_load_dwordx4 v[224:227], v[248:249], off offset:224
	global_load_dwordx4 v[228:231], v[250:251], off offset:224
	v_mbcnt_lo_u32_b32 v0, -1, 0
	v_mbcnt_hi_u32_b32 v0, -1, v0
	s_and_b32 s5, s34, 31
	v_add_u32_e32 v114, s67, v0
	s_cmp_eq_u32 s5, 0
	v_lshl_add_u32 v0, v114, 1, 0
	ds_read_u16 v2, v0 offset:14560
	ds_read_u16 v3, v0 offset:15600
	ds_read_u16 v4, v0 offset:16640
	ds_read_u16 v5, v0 offset:17680
	ds_read_u16 v6, v0 offset:18720
	ds_read_u16 v7, v0 offset:19760
	ds_read_u16 v8, v0 offset:20800
	ds_read_u16 v9, v0 offset:21840
	s_waitcnt lgkmcnt(7)
	v_lshlrev_b32_e32 v115, 16, v2
	s_waitcnt lgkmcnt(6)
	v_lshlrev_b32_e32 v49, 16, v3
	s_waitcnt lgkmcnt(5)
	v_lshlrev_b32_e32 v46, 16, v4
	s_waitcnt lgkmcnt(4)
	v_lshlrev_b32_e32 v43, 16, v5
	s_waitcnt lgkmcnt(3)
	v_lshlrev_b32_e32 v41, 16, v6
	s_waitcnt lgkmcnt(2)
	v_lshlrev_b32_e32 v38, 16, v7
	s_waitcnt lgkmcnt(1)
	v_lshlrev_b32_e32 v35, 16, v8
	s_waitcnt lgkmcnt(0)
	v_lshlrev_b32_e32 v32, 16, v9
	ds_read_u16 v2, v0 offset:22880
	ds_read_u16 v3, v0 offset:23920
	ds_read_u16 v4, v0 offset:24960
	ds_read_u16 v5, v0 offset:26000
	ds_read_u16 v6, v0 offset:27040
	ds_read_u16 v7, v0 offset:28080
	ds_read_u16 v8, v0 offset:29120
	ds_read_u16 v9, v0 offset:30160
	s_waitcnt lgkmcnt(7)
	v_lshlrev_b32_e32 v39, 16, v2
	s_waitcnt lgkmcnt(6)
	v_lshlrev_b32_e32 v36, 16, v3
	s_waitcnt lgkmcnt(5)
	v_lshlrev_b32_e32 v33, 16, v4
	s_waitcnt lgkmcnt(4)
	v_lshlrev_b32_e32 v29, 16, v5
	s_waitcnt lgkmcnt(3)
	v_lshlrev_b32_e32 v26, 16, v6
	v_add_u32_e32 v2, 0x10400, v0
	v_add_u32_e32 v3, 0x10810, v0
	v_add_u32_e32 v4, 0x10c20, v0
	v_add_u32_e32 v5, 0x11030, v0
	v_add_u32_e32 v6, 0x11440, v0
	s_waitcnt lgkmcnt(2)
	v_lshlrev_b32_e32 v24, 16, v7
	s_waitcnt lgkmcnt(1)
	v_lshlrev_b32_e32 v22, 16, v8
	s_waitcnt lgkmcnt(0)
	v_lshlrev_b32_e32 v20, 16, v9
	v_add_u32_e32 v7, 0x11850, v0
	ds_read_u16 v8, v0 offset:31200
	ds_read_u16 v9, v0 offset:32240
	ds_read_u16 v2, v2
	ds_read_u16 v3, v3
	ds_read_u16 v4, v4
	ds_read_u16 v5, v5
	ds_read_u16 v6, v6
	ds_read_u16 v10, v7
	s_waitcnt lgkmcnt(7)
	v_lshlrev_b32_e32 v64, 16, v8
	s_waitcnt lgkmcnt(6)
	v_lshlrev_b32_e32 v62, 16, v9
	ds_read_u16 v7, v0 offset:33280
	ds_read_u16 v8, v0 offset:34320
	ds_read_u16 v9, v0 offset:35360
	ds_read_u16 v11, v0 offset:36400
	ds_read_u16 v12, v0 offset:37440
	ds_read_u16 v13, v0 offset:38480
	ds_read_u16 v14, v0 offset:39520
	ds_read_u16 v15, v0 offset:40560
	s_waitcnt lgkmcnt(7)
	v_lshlrev_b32_e32 v65, 16, v7
	s_waitcnt lgkmcnt(6)
	v_lshlrev_b32_e32 v63, 16, v8
	s_waitcnt lgkmcnt(5)
	v_lshlrev_b32_e32 v61, 16, v9
	s_waitcnt lgkmcnt(4)
	v_lshlrev_b32_e32 v60, 16, v11
	s_waitcnt lgkmcnt(3)
	v_lshlrev_b32_e32 v59, 16, v12
	s_waitcnt lgkmcnt(2)
	v_lshlrev_b32_e32 v58, 16, v13
	s_waitcnt lgkmcnt(1)
	v_lshlrev_b32_e32 v56, 16, v14
	s_waitcnt lgkmcnt(0)
	v_lshlrev_b32_e32 v54, 16, v15
	ds_read_u16 v7, v0 offset:41600
	ds_read_u16 v8, v0 offset:42640
	ds_read_u16 v9, v0 offset:43680
	ds_read_u16 v11, v0 offset:44720
	ds_read_u16 v12, v0 offset:45760
	ds_read_u16 v13, v0 offset:46800
	ds_read_u16 v14, v0 offset:47840
	ds_read_u16 v15, v0 offset:48880
	s_waitcnt lgkmcnt(7)
	v_lshlrev_b32_e32 v57, 16, v7
	s_waitcnt lgkmcnt(6)
	v_lshlrev_b32_e32 v55, 16, v8
	s_waitcnt lgkmcnt(5)
	v_lshlrev_b32_e32 v53, 16, v9
	s_waitcnt lgkmcnt(4)
	v_lshlrev_b32_e32 v52, 16, v11
	s_waitcnt lgkmcnt(3)
	v_lshlrev_b32_e32 v51, 16, v12
	s_waitcnt lgkmcnt(2)
	v_lshlrev_b32_e32 v50, 16, v13
	s_waitcnt lgkmcnt(1)
	v_lshlrev_b32_e32 v47, 16, v14
	s_waitcnt lgkmcnt(0)
	v_lshlrev_b32_e32 v44, 16, v15
	ds_read_u16 v7, v0 offset:49920
	ds_read_u16 v8, v0 offset:50960
	ds_read_u16 v9, v0 offset:52000
	ds_read_u16 v11, v0 offset:53040
	ds_read_u16 v12, v0 offset:54080
	ds_read_u16 v13, v0 offset:55120
	ds_read_u16 v14, v0 offset:56160
	ds_read_u16 v15, v0 offset:57200
	s_waitcnt lgkmcnt(7)
	v_lshlrev_b32_e32 v48, 16, v7
	s_waitcnt lgkmcnt(6)
	v_lshlrev_b32_e32 v45, 16, v8
	s_waitcnt lgkmcnt(5)
	v_lshlrev_b32_e32 v42, 16, v9
	s_waitcnt lgkmcnt(4)
	v_lshlrev_b32_e32 v40, 16, v11
	s_waitcnt lgkmcnt(3)
	v_lshlrev_b32_e32 v37, 16, v12
	s_waitcnt lgkmcnt(2)
	v_lshlrev_b32_e32 v34, 16, v13
	s_waitcnt lgkmcnt(1)
	v_lshlrev_b32_e32 v30, 16, v14
	s_waitcnt lgkmcnt(0)
	v_lshlrev_b32_e32 v27, 16, v15
	ds_read_u16 v7, v0 offset:58240
	ds_read_u16 v8, v0 offset:59280
	ds_read_u16 v9, v0 offset:60320
	ds_read_u16 v11, v0 offset:61360
	ds_read_u16 v12, v0 offset:62400
	ds_read_u16 v13, v0 offset:63440
	ds_read_u16 v14, v0 offset:64480
	ds_read_u16 v15, v0 offset:65520
	s_waitcnt lgkmcnt(7)
	v_lshlrev_b32_e32 v31, 16, v7
	s_waitcnt lgkmcnt(6)
	v_lshlrev_b32_e32 v28, 16, v8
	s_waitcnt lgkmcnt(5)
	v_lshlrev_b32_e32 v25, 16, v9
	s_waitcnt lgkmcnt(3)
	v_lshlrev_b32_e32 v21, 16, v12
	s_waitcnt lgkmcnt(1)
	v_lshlrev_b32_e32 v18, 16, v14
	v_lshlrev_b32_e32 v14, 16, v2
	v_lshlrev_b32_e32 v12, 16, v3
	v_lshlrev_b32_e32 v9, 16, v4
	v_lshlrev_b32_e32 v7, 16, v5
	v_lshlrev_b32_e32 v5, 16, v6
	v_lshlrev_b32_e32 v3, 16, v10
	v_add_u32_e32 v2, 0x11c60, v0
	v_add_u32_e32 v4, 0x12070, v0
	v_add_u32_e32 v6, 0x12480, v0
	v_add_u32_e32 v8, 0x12890, v0
	v_add_u32_e32 v10, 0x12ca0, v0
	v_lshlrev_b32_e32 v23, 16, v11
	v_lshlrev_b32_e32 v19, 16, v13
	s_waitcnt lgkmcnt(0)
	v_lshlrev_b32_e32 v16, 16, v15
	v_add_u32_e32 v11, 0x130b0, v0
	v_add_u32_e32 v13, 0x134c0, v0
	v_add_u32_e32 v15, 0x138d0, v0
	ds_read_u16 v2, v2
	ds_read_u16 v4, v4
	ds_read_u16 v6, v6
	ds_read_u16 v8, v8
	ds_read_u16 v10, v10
	ds_read_u16 v122, v11
	ds_read_u16 v123, v13
	ds_read_u16 v124, v15
	s_waitcnt lgkmcnt(7)
	v_lshlrev_b32_e32 v17, 16, v2
	v_add_u32_e32 v2, 0x13ce0, v0
	ds_read_u16 v2, v2
	v_readfirstlane_b32 s4, v114
	v_add_f32_e32 v114, 0, v49
	s_waitcnt lgkmcnt(7)
	v_lshlrev_b32_e32 v15, 16, v4
	s_waitcnt lgkmcnt(6)
	v_lshlrev_b32_e32 v13, 16, v6
	s_waitcnt lgkmcnt(5)
	v_lshlrev_b32_e32 v11, 16, v8
	s_waitcnt lgkmcnt(4)
	v_lshlrev_b32_e32 v10, 16, v10
	s_waitcnt lgkmcnt(3)
	v_lshlrev_b32_e32 v8, 16, v122
	s_waitcnt lgkmcnt(2)
	v_lshlrev_b32_e32 v6, 16, v123
	s_waitcnt lgkmcnt(1)
	v_lshlrev_b32_e32 v4, 16, v124
	s_waitcnt lgkmcnt(0)
	v_lshlrev_b32_e32 v2, 16, v2
	s_cselect_b64 s[6:7], -1, 0
	s_mov_b64 s[8:9], -1
	s_cmpk_gt_u32 s4, 0x7f
	v_add_f32_e32 v114, v114, v115
	s_cbranch_scc0 .LBB0_595
	ds_read_u16 v129, v0
	ds_read_u16 v130, v0 offset:1040
	ds_read_u16 v131, v0 offset:2080
	ds_read_u16 v132, v0 offset:3120
	ds_read_u16 v133, v0 offset:4160
	ds_read_u16 v134, v0 offset:5200
	ds_read_u16 v135, v0 offset:6240
	ds_read_u16 v136, v0 offset:7280
	ds_read_u16 v122, v0 offset:12480
	ds_read_u16 v123, v0 offset:13520
	ds_read_u16 v125, v0 offset:8320
	ds_read_u16 v126, v0 offset:9360
	ds_read_u16 v137, v0 offset:10400
	ds_read_u16 v138, v0 offset:11440
	s_waitcnt lgkmcnt(5)
	v_lshlrev_b32_e32 v124, 16, v122
	s_waitcnt lgkmcnt(4)
	v_lshlrev_b32_e32 v122, 16, v123
	s_ashr_i32 s14, s4, 7
	v_add_f32_e32 v123, v114, v122
	v_add_f32_e32 v123, v123, v124
	s_waitcnt lgkmcnt(3)
	v_lshlrev_b32_e32 v128, 16, v125
	s_waitcnt lgkmcnt(2)
	v_lshlrev_b32_e32 v127, 16, v126
	s_waitcnt lgkmcnt(1)
	v_lshlrev_b32_e32 v126, 16, v137
	s_waitcnt lgkmcnt(0)
	v_lshlrev_b32_e32 v125, 16, v138
	s_mov_b64 s[12:13], -1
	s_mov_b64 s[8:9], 0
	s_cmp_lt_i32 s14, 2
	s_mov_b64 s[10:11], 0
	s_cbranch_scc1 .LBB0_590
	s_cmp_eq_u32 s14, 2
	s_mov_b64 s[10:11], -1
	s_cbranch_scc0 .LBB0_587
	v_add_f32_e32 v137, v123, v125
	v_add_f32_e32 v137, v137, v126
	v_add_f32_e32 v137, v137, v127
	v_mov_b32_e32 v139, 0x3e000000
	v_add_f32_e32 v137, v137, v128
	v_cndmask_b32_e64 v138, v139, 1.0, s[6:7]
	v_fma_f32 v137, v138, v137, -v49
	v_cvt_pk_bf16_f32 v137, v137, s0
	ds_write_b16 v0, v137
	v_add_f32_e32 v137, 0, v46
	v_add_f32_e32 v137, v137, v49
	v_add_f32_e32 v137, v137, v115
	v_add_f32_e32 v137, v137, v122
	v_add_f32_e32 v137, v137, v124
	v_add_f32_e32 v137, v137, v125
	v_add_f32_e32 v137, v137, v126
	v_add_f32_e32 v137, v137, v127
	v_cndmask_b32_e64 v138, v139, 0.5, s[6:7]
	v_fma_f32 v137, v138, v137, -v46
	v_cvt_pk_bf16_f32 v137, v137, s0
	ds_write_b16 v0, v137 offset:1040
	v_add_f32_e32 v137, 0, v43
	v_add_f32_e32 v137, v137, v46
	v_add_f32_e32 v137, v137, v49
	v_add_f32_e32 v137, v137, v115
	v_add_f32_e32 v137, v137, v122
	v_add_f32_e32 v137, v137, v124
	v_add_f32_e32 v137, v137, v125
	v_mov_b32_e32 v138, 0x3eaaaaab
	v_add_f32_e32 v137, v137, v126
	v_cndmask_b32_e64 v138, v139, v138, s[6:7]
	v_fma_f32 v137, v138, v137, -v43
	v_cvt_pk_bf16_f32 v137, v137, s0
	ds_write_b16 v0, v137 offset:2080
	v_add_f32_e32 v137, 0, v41
	v_add_f32_e32 v137, v137, v43
	v_add_f32_e32 v137, v137, v46
	v_add_f32_e32 v137, v137, v49
	v_add_f32_e32 v137, v137, v115
	v_add_f32_e32 v137, v137, v122
	v_add_f32_e32 v137, v137, v124
	v_mov_b32_e32 v138, 0x3e800000
	v_add_f32_e32 v137, v137, v125
	v_cndmask_b32_e64 v138, v139, v138, s[6:7]
	v_fma_f32 v137, v138, v137, -v41
	v_cvt_pk_bf16_f32 v137, v137, s0
	ds_write_b16 v0, v137 offset:3120
	v_add_f32_e32 v137, 0, v38
	v_add_f32_e32 v137, v137, v41
	v_add_f32_e32 v137, v137, v43
	v_add_f32_e32 v137, v137, v46
	v_add_f32_e32 v137, v137, v49
	v_add_f32_e32 v137, v137, v115
	v_add_f32_e32 v137, v137, v122
	v_mov_b32_e32 v138, 0x3e4ccccd
	v_add_f32_e32 v137, v137, v124
	v_cndmask_b32_e64 v138, v139, v138, s[6:7]
	v_fma_f32 v137, v138, v137, -v38
	v_cvt_pk_bf16_f32 v137, v137, s0
	ds_write_b16 v0, v137 offset:4160
	v_add_f32_e32 v137, 0, v35
	v_add_f32_e32 v137, v137, v38
	v_add_f32_e32 v137, v137, v41
	v_add_f32_e32 v137, v137, v43
	v_add_f32_e32 v137, v137, v46
	v_add_f32_e32 v137, v137, v49
	v_add_f32_e32 v137, v137, v115
	v_mov_b32_e32 v138, 0x3e2aaaab
	v_add_f32_e32 v137, v137, v122
	v_cndmask_b32_e64 v138, v139, v138, s[6:7]
	v_fma_f32 v137, v138, v137, -v35
	v_cvt_pk_bf16_f32 v137, v137, s0
	ds_write_b16 v0, v137 offset:5200
	v_add_f32_e32 v137, 0, v32
	v_add_f32_e32 v137, v137, v35
	v_add_f32_e32 v137, v137, v38
	v_add_f32_e32 v137, v137, v41
	v_add_f32_e32 v137, v137, v43
	v_add_f32_e32 v137, v137, v46
	v_add_f32_e32 v137, v137, v49
	v_mov_b32_e32 v138, 0x3e124925
	v_add_f32_e32 v137, v137, v115
	v_cndmask_b32_e64 v138, v139, v138, s[6:7]
	v_fma_f32 v137, v138, v137, -v32
	v_cvt_pk_bf16_f32 v137, v137, s0
	ds_write_b16 v0, v137 offset:6240
	v_add_f32_e32 v137, 0, v39
	v_add_f32_e32 v137, v137, v32
	v_add_f32_e32 v137, v137, v35
	v_add_f32_e32 v137, v137, v38
	v_add_f32_e32 v137, v137, v41
	v_add_f32_e32 v137, v137, v43
	v_add_f32_e32 v137, v137, v46
	v_add_f32_e32 v137, v137, v49
	s_mov_b32 s4, 0x3e000000
	v_fma_f32 v137, v137, s4, -v39
	v_cvt_pk_bf16_f32 v137, v137, s0
	ds_write_b16 v0, v137 offset:7280
	v_add_f32_e32 v137, 0, v36
	v_add_f32_e32 v137, v137, v39
	v_add_f32_e32 v137, v137, v32
	v_add_f32_e32 v137, v137, v35
	v_add_f32_e32 v137, v137, v38
	v_add_f32_e32 v137, v137, v41
	v_add_f32_e32 v137, v137, v43
	v_add_f32_e32 v137, v137, v46
	v_fma_f32 v137, v137, s4, -v36
	v_cvt_pk_bf16_f32 v137, v137, s0
	ds_write_b16 v0, v137 offset:8320
	v_add_f32_e32 v137, 0, v33
	v_add_f32_e32 v137, v137, v36
	v_add_f32_e32 v137, v137, v39
	v_add_f32_e32 v137, v137, v32
	v_add_f32_e32 v137, v137, v35
	v_add_f32_e32 v137, v137, v38
	v_add_f32_e32 v137, v137, v41
	v_add_f32_e32 v137, v137, v43
	v_fma_f32 v137, v137, s4, -v33
	v_cvt_pk_bf16_f32 v137, v137, s0
	ds_write_b16 v0, v137 offset:9360
	v_add_f32_e32 v137, 0, v29
	v_add_f32_e32 v137, v137, v33
	v_add_f32_e32 v137, v137, v36
	v_add_f32_e32 v137, v137, v39
	v_add_f32_e32 v137, v137, v32
	v_add_f32_e32 v137, v137, v35
	v_add_f32_e32 v137, v137, v38
	v_add_f32_e32 v137, v137, v41
	v_fma_f32 v137, v137, s4, -v29
	v_cvt_pk_bf16_f32 v137, v137, s0
	ds_write_b16 v0, v137 offset:10400
	v_add_f32_e32 v137, 0, v26
	v_add_f32_e32 v137, v137, v29
	v_add_f32_e32 v137, v137, v33
	v_add_f32_e32 v137, v137, v36
	v_add_f32_e32 v137, v137, v39
	v_add_f32_e32 v137, v137, v32
	v_add_f32_e32 v137, v137, v35
	v_add_f32_e32 v137, v137, v38
	v_fma_f32 v137, v137, s4, -v26
	v_cvt_pk_bf16_f32 v137, v137, s0
	ds_write_b16 v0, v137 offset:11440
	v_add_f32_e32 v137, 0, v24
	v_add_f32_e32 v137, v137, v26
	v_add_f32_e32 v137, v137, v29
	v_add_f32_e32 v137, v137, v33
	v_add_f32_e32 v137, v137, v36
	v_add_f32_e32 v137, v137, v39
	v_add_f32_e32 v137, v137, v32
	v_add_f32_e32 v137, v137, v35
	v_fma_f32 v137, v137, s4, -v24
	v_cvt_pk_bf16_f32 v137, v137, s0
	ds_write_b16 v0, v137 offset:12480
	v_add_f32_e32 v137, 0, v22
	v_add_f32_e32 v137, v137, v24
	v_add_f32_e32 v137, v137, v26
	v_add_f32_e32 v137, v137, v29
	v_add_f32_e32 v137, v137, v33
	v_add_f32_e32 v137, v137, v36
	v_add_f32_e32 v137, v137, v39
	v_add_f32_e32 v137, v137, v32
	v_fma_f32 v137, v137, s4, -v22
	v_cvt_pk_bf16_f32 v137, v137, s0
	ds_write_b16 v0, v137 offset:13520
	v_add_f32_e32 v137, 0, v20
	v_add_f32_e32 v137, v137, v22
	v_add_f32_e32 v137, v137, v24
	v_add_f32_e32 v137, v137, v26
	v_add_f32_e32 v137, v137, v29
	v_add_f32_e32 v137, v137, v33
	v_add_f32_e32 v137, v137, v36
	v_add_f32_e32 v137, v137, v39
	v_fma_f32 v137, v137, s4, -v20
	v_cvt_pk_bf16_f32 v137, v137, s0
	ds_write_b16 v0, v137 offset:14560
	v_add_f32_e32 v137, 0, v64
	v_add_f32_e32 v137, v137, v20
	v_add_f32_e32 v137, v137, v22
	v_add_f32_e32 v137, v137, v24
	v_add_f32_e32 v137, v137, v26
	v_add_f32_e32 v137, v137, v29
	v_add_f32_e32 v137, v137, v33
	v_add_f32_e32 v137, v137, v36
	v_fma_f32 v137, v137, s4, -v64
	v_cvt_pk_bf16_f32 v137, v137, s0
	ds_write_b16 v0, v137 offset:15600
	v_add_f32_e32 v137, 0, v62
	v_add_f32_e32 v137, v137, v64
	v_add_f32_e32 v137, v137, v20
	v_add_f32_e32 v137, v137, v22
	v_add_f32_e32 v137, v137, v24
	v_add_f32_e32 v137, v137, v26
	v_add_f32_e32 v137, v137, v29
	v_add_f32_e32 v137, v137, v33
	v_fma_f32 v137, v137, s4, -v62
	v_cvt_pk_bf16_f32 v137, v137, s0
	ds_write_b16 v0, v137 offset:16640
	v_add_f32_e32 v137, 0, v65
	v_add_f32_e32 v137, v137, v62
	v_add_f32_e32 v137, v137, v64
	v_add_f32_e32 v137, v137, v20
	v_add_f32_e32 v137, v137, v22
	v_add_f32_e32 v137, v137, v24
	v_add_f32_e32 v137, v137, v26
	v_add_f32_e32 v137, v137, v29
	v_fma_f32 v137, v137, s4, -v65
	v_cvt_pk_bf16_f32 v137, v137, s0
	ds_write_b16 v0, v137 offset:17680
	v_add_f32_e32 v137, 0, v63
	v_add_f32_e32 v137, v137, v65
	v_add_f32_e32 v137, v137, v62
	v_add_f32_e32 v137, v137, v64
	v_add_f32_e32 v137, v137, v20
	v_add_f32_e32 v137, v137, v22
	v_add_f32_e32 v137, v137, v24
	v_add_f32_e32 v137, v137, v26
	v_fma_f32 v137, v137, s4, -v63
	v_cvt_pk_bf16_f32 v137, v137, s0
	ds_write_b16 v0, v137 offset:18720
	v_add_f32_e32 v137, 0, v61
	v_add_f32_e32 v137, v137, v63
	v_add_f32_e32 v137, v137, v65
	v_add_f32_e32 v137, v137, v62
	v_add_f32_e32 v137, v137, v64
	v_add_f32_e32 v137, v137, v20
	v_add_f32_e32 v137, v137, v22
	v_add_f32_e32 v137, v137, v24
	v_fma_f32 v137, v137, s4, -v61
	v_cvt_pk_bf16_f32 v137, v137, s0
	ds_write_b16 v0, v137 offset:19760
	v_add_f32_e32 v137, 0, v60
	v_add_f32_e32 v137, v137, v61
	v_add_f32_e32 v137, v137, v63
	v_add_f32_e32 v137, v137, v65
	v_add_f32_e32 v137, v137, v62
	v_add_f32_e32 v137, v137, v64
	v_add_f32_e32 v137, v137, v20
	v_add_f32_e32 v137, v137, v22
	v_fma_f32 v137, v137, s4, -v60
	v_cvt_pk_bf16_f32 v137, v137, s0
	ds_write_b16 v0, v137 offset:20800
	v_add_f32_e32 v137, 0, v59
	v_add_f32_e32 v137, v137, v60
	v_add_f32_e32 v137, v137, v61
	v_add_f32_e32 v137, v137, v63
	v_add_f32_e32 v137, v137, v65
	v_add_f32_e32 v137, v137, v62
	v_add_f32_e32 v137, v137, v64
	v_add_f32_e32 v137, v137, v20
	v_fma_f32 v137, v137, s4, -v59
	v_cvt_pk_bf16_f32 v137, v137, s0
	ds_write_b16 v0, v137 offset:21840
	v_add_f32_e32 v137, 0, v58
	v_add_f32_e32 v137, v137, v59
	v_add_f32_e32 v137, v137, v60
	v_add_f32_e32 v137, v137, v61
	v_add_f32_e32 v137, v137, v63
	v_add_f32_e32 v137, v137, v65
	v_add_f32_e32 v137, v137, v62
	v_add_f32_e32 v137, v137, v64
	v_fma_f32 v137, v137, s4, -v58
	v_cvt_pk_bf16_f32 v137, v137, s0
	ds_write_b16 v0, v137 offset:22880
	v_add_f32_e32 v137, 0, v56
	v_add_f32_e32 v137, v137, v58
	v_add_f32_e32 v137, v137, v59
	v_add_f32_e32 v137, v137, v60
	v_add_f32_e32 v137, v137, v61
	v_add_f32_e32 v137, v137, v63
	v_add_f32_e32 v137, v137, v65
	v_add_f32_e32 v137, v137, v62
	v_fma_f32 v137, v137, s4, -v56
	v_cvt_pk_bf16_f32 v137, v137, s0
	ds_write_b16 v0, v137 offset:23920
	v_add_f32_e32 v137, 0, v54
	v_add_f32_e32 v137, v137, v56
	v_add_f32_e32 v137, v137, v58
	v_add_f32_e32 v137, v137, v59
	v_add_f32_e32 v137, v137, v60
	v_add_f32_e32 v137, v137, v61
	v_add_f32_e32 v137, v137, v63
	v_add_f32_e32 v137, v137, v65
	v_fma_f32 v137, v137, s4, -v54
	v_cvt_pk_bf16_f32 v137, v137, s0
	ds_write_b16 v0, v137 offset:24960
	v_add_f32_e32 v137, 0, v57
	v_add_f32_e32 v137, v137, v54
	v_add_f32_e32 v137, v137, v56
	v_add_f32_e32 v137, v137, v58
	v_add_f32_e32 v137, v137, v59
	v_add_f32_e32 v137, v137, v60
	v_add_f32_e32 v137, v137, v61
	v_add_f32_e32 v137, v137, v63
	v_fma_f32 v137, v137, s4, -v57
	v_cvt_pk_bf16_f32 v137, v137, s0
	ds_write_b16 v0, v137 offset:26000
	v_add_f32_e32 v137, 0, v55
	v_add_f32_e32 v137, v137, v57
	v_add_f32_e32 v137, v137, v54
	v_add_f32_e32 v137, v137, v56
	v_add_f32_e32 v137, v137, v58
	v_add_f32_e32 v137, v137, v59
	v_add_f32_e32 v137, v137, v60
	v_add_f32_e32 v137, v137, v61
	v_fma_f32 v137, v137, s4, -v55
	v_cvt_pk_bf16_f32 v137, v137, s0
	ds_write_b16 v0, v137 offset:27040
	v_add_f32_e32 v137, 0, v53
	v_add_f32_e32 v137, v137, v55
	v_add_f32_e32 v137, v137, v57
	v_add_f32_e32 v137, v137, v54
	v_add_f32_e32 v137, v137, v56
	v_add_f32_e32 v137, v137, v58
	v_add_f32_e32 v137, v137, v59
	v_add_f32_e32 v137, v137, v60
	v_fma_f32 v137, v137, s4, -v53
	v_cvt_pk_bf16_f32 v137, v137, s0
	ds_write_b16 v0, v137 offset:28080
	v_add_f32_e32 v137, 0, v52
	v_add_f32_e32 v137, v137, v53
	v_add_f32_e32 v137, v137, v55
	v_add_f32_e32 v137, v137, v57
	v_add_f32_e32 v137, v137, v54
	v_add_f32_e32 v137, v137, v56
	v_add_f32_e32 v137, v137, v58
	v_add_f32_e32 v137, v137, v59
	v_fma_f32 v137, v137, s4, -v52
	v_cvt_pk_bf16_f32 v137, v137, s0
	ds_write_b16 v0, v137 offset:29120
	v_add_f32_e32 v137, 0, v51
	v_add_f32_e32 v137, v137, v52
	v_add_f32_e32 v137, v137, v53
	v_add_f32_e32 v137, v137, v55
	v_add_f32_e32 v137, v137, v57
	v_add_f32_e32 v137, v137, v54
	v_add_f32_e32 v137, v137, v56
	v_add_f32_e32 v137, v137, v58
	v_fma_f32 v137, v137, s4, -v51
	v_cvt_pk_bf16_f32 v137, v137, s0
	ds_write_b16 v0, v137 offset:30160
	v_add_f32_e32 v137, 0, v50
	v_add_f32_e32 v137, v137, v51
	v_add_f32_e32 v137, v137, v52
	v_add_f32_e32 v137, v137, v53
	v_add_f32_e32 v137, v137, v55
	v_add_f32_e32 v137, v137, v57
	v_add_f32_e32 v137, v137, v54
	v_add_f32_e32 v137, v137, v56
	v_fma_f32 v137, v137, s4, -v50
	v_cvt_pk_bf16_f32 v137, v137, s0
	ds_write_b16 v0, v137 offset:31200
	v_add_f32_e32 v137, 0, v47
	v_add_f32_e32 v137, v137, v50
	v_add_f32_e32 v137, v137, v51
	v_add_f32_e32 v137, v137, v52
	v_add_f32_e32 v137, v137, v53
	v_add_f32_e32 v137, v137, v55
	v_add_f32_e32 v137, v137, v57
	v_add_f32_e32 v137, v137, v54
	v_fma_f32 v137, v137, s4, -v47
	v_cvt_pk_bf16_f32 v137, v137, s0
	ds_write_b16 v0, v137 offset:32240
	v_add_f32_e32 v137, 0, v44
	v_add_f32_e32 v137, v137, v47
	v_add_f32_e32 v137, v137, v50
	v_add_f32_e32 v137, v137, v51
	v_add_f32_e32 v137, v137, v52
	v_add_f32_e32 v137, v137, v53
	v_add_f32_e32 v137, v137, v55
	v_add_f32_e32 v137, v137, v57
	v_fma_f32 v137, v137, s4, -v44
	v_cvt_pk_bf16_f32 v137, v137, s0
	ds_write_b16 v0, v137 offset:33280
	v_add_f32_e32 v137, 0, v48
	v_add_f32_e32 v137, v137, v44
	v_add_f32_e32 v137, v137, v47
	v_add_f32_e32 v137, v137, v50
	v_add_f32_e32 v137, v137, v51
	v_add_f32_e32 v137, v137, v52
	v_add_f32_e32 v137, v137, v53
	v_add_f32_e32 v137, v137, v55
	v_fma_f32 v137, v137, s4, -v48
	v_cvt_pk_bf16_f32 v137, v137, s0
	ds_write_b16 v0, v137 offset:34320
	v_add_f32_e32 v137, 0, v45
	v_add_f32_e32 v137, v137, v48
	v_add_f32_e32 v137, v137, v44
	v_add_f32_e32 v137, v137, v47
	v_add_f32_e32 v137, v137, v50
	v_add_f32_e32 v137, v137, v51
	v_add_f32_e32 v137, v137, v52
	v_add_f32_e32 v137, v137, v53
	v_fma_f32 v137, v137, s4, -v45
	v_cvt_pk_bf16_f32 v137, v137, s0
	ds_write_b16 v0, v137 offset:35360
	v_add_f32_e32 v137, 0, v42
	v_add_f32_e32 v137, v137, v45
	v_add_f32_e32 v137, v137, v48
	v_add_f32_e32 v137, v137, v44
	v_add_f32_e32 v137, v137, v47
	v_add_f32_e32 v137, v137, v50
	v_add_f32_e32 v137, v137, v51
	v_add_f32_e32 v137, v137, v52
	v_fma_f32 v137, v137, s4, -v42
	v_cvt_pk_bf16_f32 v137, v137, s0
	ds_write_b16 v0, v137 offset:36400
	v_add_f32_e32 v137, 0, v40
	v_add_f32_e32 v137, v137, v42
	v_add_f32_e32 v137, v137, v45
	v_add_f32_e32 v137, v137, v48
	v_add_f32_e32 v137, v137, v44
	v_add_f32_e32 v137, v137, v47
	v_add_f32_e32 v137, v137, v50
	v_add_f32_e32 v137, v137, v51
	v_fma_f32 v137, v137, s4, -v40
	v_cvt_pk_bf16_f32 v137, v137, s0
	ds_write_b16 v0, v137 offset:37440
	v_add_f32_e32 v137, 0, v37
	v_add_f32_e32 v137, v137, v40
	v_add_f32_e32 v137, v137, v42
	v_add_f32_e32 v137, v137, v45
	v_add_f32_e32 v137, v137, v48
	v_add_f32_e32 v137, v137, v44
	v_add_f32_e32 v137, v137, v47
	v_add_f32_e32 v137, v137, v50
	v_fma_f32 v137, v137, s4, -v37
	v_cvt_pk_bf16_f32 v137, v137, s0
	ds_write_b16 v0, v137 offset:38480
	v_add_f32_e32 v137, 0, v34
	v_add_f32_e32 v137, v137, v37
	v_add_f32_e32 v137, v137, v40
	v_add_f32_e32 v137, v137, v42
	v_add_f32_e32 v137, v137, v45
	v_add_f32_e32 v137, v137, v48
	v_add_f32_e32 v137, v137, v44
	v_add_f32_e32 v137, v137, v47
	v_fma_f32 v137, v137, s4, -v34
	v_cvt_pk_bf16_f32 v137, v137, s0
	ds_write_b16 v0, v137 offset:39520
	v_add_f32_e32 v137, 0, v30
	v_add_f32_e32 v137, v137, v34
	v_add_f32_e32 v137, v137, v37
	v_add_f32_e32 v137, v137, v40
	v_add_f32_e32 v137, v137, v42
	v_add_f32_e32 v137, v137, v45
	v_add_f32_e32 v137, v137, v48
	v_add_f32_e32 v137, v137, v44
	v_fma_f32 v137, v137, s4, -v30
	v_cvt_pk_bf16_f32 v137, v137, s0
	ds_write_b16 v0, v137 offset:40560
	v_add_f32_e32 v137, 0, v27
	v_add_f32_e32 v137, v137, v30
	v_add_f32_e32 v137, v137, v34
	v_add_f32_e32 v137, v137, v37
	v_add_f32_e32 v137, v137, v40
	v_add_f32_e32 v137, v137, v42
	v_add_f32_e32 v137, v137, v45
	v_add_f32_e32 v137, v137, v48
	v_fma_f32 v137, v137, s4, -v27
	v_cvt_pk_bf16_f32 v137, v137, s0
	ds_write_b16 v0, v137 offset:41600
	v_add_f32_e32 v137, 0, v31
	v_add_f32_e32 v137, v137, v27
	v_add_f32_e32 v137, v137, v30
	v_add_f32_e32 v137, v137, v34
	v_add_f32_e32 v137, v137, v37
	v_add_f32_e32 v137, v137, v40
	v_add_f32_e32 v137, v137, v42
	v_add_f32_e32 v137, v137, v45
	v_fma_f32 v137, v137, s4, -v31
	v_cvt_pk_bf16_f32 v137, v137, s0
	ds_write_b16 v0, v137 offset:42640
	v_add_f32_e32 v137, 0, v28
	v_add_f32_e32 v137, v137, v31
	v_add_f32_e32 v137, v137, v27
	v_add_f32_e32 v137, v137, v30
	v_add_f32_e32 v137, v137, v34
	v_add_f32_e32 v137, v137, v37
	v_add_f32_e32 v137, v137, v40
	v_add_f32_e32 v137, v137, v42
	v_fma_f32 v137, v137, s4, -v28
	v_cvt_pk_bf16_f32 v137, v137, s0
	ds_write_b16 v0, v137 offset:43680
	v_add_f32_e32 v137, 0, v25
	v_add_f32_e32 v137, v137, v28
	v_add_f32_e32 v137, v137, v31
	v_add_f32_e32 v137, v137, v27
	v_add_f32_e32 v137, v137, v30
	v_add_f32_e32 v137, v137, v34
	v_add_f32_e32 v137, v137, v37
	v_add_f32_e32 v137, v137, v40
	v_fma_f32 v137, v137, s4, -v25
	v_cvt_pk_bf16_f32 v137, v137, s0
	ds_write_b16 v0, v137 offset:44720
	v_add_f32_e32 v137, 0, v23
	v_add_f32_e32 v137, v137, v25
	v_add_f32_e32 v137, v137, v28
	v_add_f32_e32 v137, v137, v31
	v_add_f32_e32 v137, v137, v27
	v_add_f32_e32 v137, v137, v30
	v_add_f32_e32 v137, v137, v34
	v_add_f32_e32 v137, v137, v37
	v_fma_f32 v137, v137, s4, -v23
	v_cvt_pk_bf16_f32 v137, v137, s0
	ds_write_b16 v0, v137 offset:45760
	v_add_f32_e32 v137, 0, v21
	v_add_f32_e32 v137, v137, v23
	v_add_f32_e32 v137, v137, v25
	v_add_f32_e32 v137, v137, v28
	v_add_f32_e32 v137, v137, v31
	v_add_f32_e32 v137, v137, v27
	v_add_f32_e32 v137, v137, v30
	v_add_f32_e32 v137, v137, v34
	v_fma_f32 v137, v137, s4, -v21
	v_cvt_pk_bf16_f32 v137, v137, s0
	ds_write_b16 v0, v137 offset:46800
	v_add_f32_e32 v137, 0, v19
	v_add_f32_e32 v137, v137, v21
	v_add_f32_e32 v137, v137, v23
	v_add_f32_e32 v137, v137, v25
	v_add_f32_e32 v137, v137, v28
	v_add_f32_e32 v137, v137, v31
	v_add_f32_e32 v137, v137, v27
	v_add_f32_e32 v137, v137, v30
	v_fma_f32 v137, v137, s4, -v19
	v_cvt_pk_bf16_f32 v137, v137, s0
	ds_write_b16 v0, v137 offset:47840
	v_add_f32_e32 v137, 0, v18
	v_add_f32_e32 v137, v137, v19
	v_add_f32_e32 v137, v137, v21
	v_add_f32_e32 v137, v137, v23
	v_add_f32_e32 v137, v137, v25
	v_add_f32_e32 v137, v137, v28
	v_add_f32_e32 v137, v137, v31
	v_add_f32_e32 v137, v137, v27
	v_fma_f32 v137, v137, s4, -v18
	v_cvt_pk_bf16_f32 v137, v137, s0
	ds_write_b16 v0, v137 offset:48880
	v_add_f32_e32 v137, 0, v16
	v_add_f32_e32 v137, v137, v18
	v_add_f32_e32 v137, v137, v19
	v_add_f32_e32 v137, v137, v21
	v_add_f32_e32 v137, v137, v23
	v_add_f32_e32 v137, v137, v25
	v_add_f32_e32 v137, v137, v28
	v_add_f32_e32 v137, v137, v31
	v_fma_f32 v137, v137, s4, -v16
	v_cvt_pk_bf16_f32 v137, v137, s0
	ds_write_b16 v0, v137 offset:49920
	v_add_f32_e32 v137, 0, v14
	v_add_f32_e32 v137, v137, v16
	v_add_f32_e32 v137, v137, v18
	v_add_f32_e32 v137, v137, v19
	v_add_f32_e32 v137, v137, v21
	v_add_f32_e32 v137, v137, v23
	v_add_f32_e32 v137, v137, v25
	v_add_f32_e32 v137, v137, v28
	v_fma_f32 v137, v137, s4, -v14
	v_cvt_pk_bf16_f32 v137, v137, s0
	ds_write_b16 v0, v137 offset:50960
	v_add_f32_e32 v137, 0, v12
	v_add_f32_e32 v137, v137, v14
	v_add_f32_e32 v137, v137, v16
	v_add_f32_e32 v137, v137, v18
	v_add_f32_e32 v137, v137, v19
	v_add_f32_e32 v137, v137, v21
	v_add_f32_e32 v137, v137, v23
	v_add_f32_e32 v137, v137, v25
	v_fma_f32 v137, v137, s4, -v12
	v_cvt_pk_bf16_f32 v137, v137, s0
	ds_write_b16 v0, v137 offset:52000
	v_add_f32_e32 v137, 0, v9
	v_add_f32_e32 v137, v137, v12
	v_add_f32_e32 v137, v137, v14
	v_add_f32_e32 v137, v137, v16
	v_add_f32_e32 v137, v137, v18
	v_add_f32_e32 v137, v137, v19
	v_add_f32_e32 v137, v137, v21
	v_add_f32_e32 v137, v137, v23
	v_fma_f32 v137, v137, s4, -v9
	v_cvt_pk_bf16_f32 v137, v137, s0
	ds_write_b16 v0, v137 offset:53040
	v_add_f32_e32 v137, 0, v7
	v_add_f32_e32 v137, v137, v9
	v_add_f32_e32 v137, v137, v12
	v_add_f32_e32 v137, v137, v14
	v_add_f32_e32 v137, v137, v16
	v_add_f32_e32 v137, v137, v18
	v_add_f32_e32 v137, v137, v19
	v_add_f32_e32 v137, v137, v21
	v_fma_f32 v137, v137, s4, -v7
	v_cvt_pk_bf16_f32 v137, v137, s0
	ds_write_b16 v0, v137 offset:54080
	v_add_f32_e32 v137, 0, v5
	v_add_f32_e32 v137, v137, v7
	v_add_f32_e32 v137, v137, v9
	v_add_f32_e32 v137, v137, v12
	v_add_f32_e32 v137, v137, v14
	v_add_f32_e32 v137, v137, v16
	v_add_f32_e32 v137, v137, v18
	v_add_f32_e32 v137, v137, v19
	v_fma_f32 v137, v137, s4, -v5
	v_cvt_pk_bf16_f32 v137, v137, s0
	ds_write_b16 v0, v137 offset:55120
	v_add_f32_e32 v137, 0, v3
	v_add_f32_e32 v137, v137, v5
	v_add_f32_e32 v137, v137, v7
	v_add_f32_e32 v137, v137, v9
	v_add_f32_e32 v137, v137, v12
	v_add_f32_e32 v137, v137, v14
	v_add_f32_e32 v137, v137, v16
	v_add_f32_e32 v137, v137, v18
	v_fma_f32 v137, v137, s4, -v3
	v_cvt_pk_bf16_f32 v137, v137, s0
	ds_write_b16 v0, v137 offset:56160
	v_add_f32_e32 v137, 0, v17
	v_add_f32_e32 v137, v137, v3
	v_add_f32_e32 v137, v137, v5
	v_add_f32_e32 v137, v137, v7
	v_add_f32_e32 v137, v137, v9
	v_add_f32_e32 v137, v137, v12
	v_add_f32_e32 v137, v137, v14
	v_add_f32_e32 v137, v137, v16
	v_fma_f32 v137, v137, s4, -v17
	v_cvt_pk_bf16_f32 v137, v137, s0
	ds_write_b16 v0, v137 offset:57200
	v_add_f32_e32 v137, 0, v15
	v_add_f32_e32 v137, v137, v17
	v_add_f32_e32 v137, v137, v3
	v_add_f32_e32 v137, v137, v5
	v_add_f32_e32 v137, v137, v7
	v_add_f32_e32 v137, v137, v9
	v_add_f32_e32 v137, v137, v12
	v_add_f32_e32 v137, v137, v14
	v_fma_f32 v137, v137, s4, -v15
	v_cvt_pk_bf16_f32 v137, v137, s0
	ds_write_b16 v0, v137 offset:58240
	v_add_f32_e32 v137, 0, v13
	v_add_f32_e32 v137, v137, v15
	v_add_f32_e32 v137, v137, v17
	v_add_f32_e32 v137, v137, v3
	v_add_f32_e32 v137, v137, v5
	v_add_f32_e32 v137, v137, v7
	v_add_f32_e32 v137, v137, v9
	v_add_f32_e32 v137, v137, v12
	v_fma_f32 v137, v137, s4, -v13
	v_cvt_pk_bf16_f32 v137, v137, s0
	ds_write_b16 v0, v137 offset:59280
	v_add_f32_e32 v137, 0, v11
	v_add_f32_e32 v137, v137, v13
	v_add_f32_e32 v137, v137, v15
	v_add_f32_e32 v137, v137, v17
	v_add_f32_e32 v137, v137, v3
	v_add_f32_e32 v137, v137, v5
	v_add_f32_e32 v137, v137, v7
	v_add_f32_e32 v137, v137, v9
	v_fma_f32 v137, v137, s4, -v11
	v_cvt_pk_bf16_f32 v137, v137, s0
	ds_write_b16 v0, v137 offset:60320
	v_add_f32_e32 v137, 0, v10
	v_add_f32_e32 v137, v137, v11
	v_add_f32_e32 v137, v137, v13
	v_add_f32_e32 v137, v137, v15
	v_add_f32_e32 v137, v137, v17
	v_add_f32_e32 v137, v137, v3
	v_add_f32_e32 v137, v137, v5
	v_add_f32_e32 v137, v137, v7
	v_fma_f32 v137, v137, s4, -v10
	v_cvt_pk_bf16_f32 v137, v137, s0
	ds_write_b16 v0, v137 offset:61360
	v_add_f32_e32 v137, 0, v8
	v_add_f32_e32 v137, v137, v10
	v_add_f32_e32 v137, v137, v11
	v_add_f32_e32 v137, v137, v13
	v_add_f32_e32 v137, v137, v15
	v_add_f32_e32 v137, v137, v17
	v_add_f32_e32 v137, v137, v3
	v_add_f32_e32 v137, v137, v5
	v_fma_f32 v137, v137, s4, -v8
	v_cvt_pk_bf16_f32 v137, v137, s0
	ds_write_b16 v0, v137 offset:62400
	v_add_f32_e32 v137, 0, v6
	v_add_f32_e32 v137, v137, v8
	v_add_f32_e32 v137, v137, v10
	v_add_f32_e32 v137, v137, v11
	v_add_f32_e32 v137, v137, v13
	v_add_f32_e32 v137, v137, v15
	v_add_f32_e32 v137, v137, v17
	v_add_f32_e32 v137, v137, v3
	v_fma_f32 v137, v137, s4, -v6
	v_cvt_pk_bf16_f32 v137, v137, s0
	ds_write_b16 v0, v137 offset:63440
	v_add_f32_e32 v137, 0, v4
	v_add_f32_e32 v137, v137, v6
	v_add_f32_e32 v137, v137, v8
	v_add_f32_e32 v137, v137, v10
	v_add_f32_e32 v137, v137, v11
	v_add_f32_e32 v137, v137, v13
	v_add_f32_e32 v137, v137, v15
	v_add_f32_e32 v137, v137, v17
	v_fma_f32 v137, v137, s4, -v4
	v_cvt_pk_bf16_f32 v137, v137, s0
	ds_write_b16 v0, v137 offset:64480
	v_add_f32_e32 v137, 0, v2
	v_add_f32_e32 v137, v137, v4
	v_add_f32_e32 v137, v137, v6
	v_add_f32_e32 v137, v137, v8
	v_add_f32_e32 v137, v137, v10
	v_add_f32_e32 v137, v137, v11
	v_add_f32_e32 v137, v137, v13
	v_add_f32_e32 v137, v137, v15
	v_mul_f32_e32 v137, 0x3e000000, v137
	s_mov_b64 s[10:11], 0

.LBB0_597:
	v_sub_f32_e32 v2, v137, v2
	v_cvt_pk_bf16_f32 v2, v2, s0
	s_mov_b64 s[4:5], s[0:1]
	ds_write_b16 v0, v2 offset:65520
	s_waitcnt lgkmcnt(0)
	s_barrier
	s_waitcnt vmcnt(0)
	s_load_dwordx2 s[8:9], s[4:5], 0xd0
	s_nop 0
	s_load_dwordx2 s[4:5], s[4:5], 0x68
	v_mbcnt_lo_u32_b32 v0, -1, 0
	v_mbcnt_hi_u32_b32 v0, -1, v0
	s_add_i32 s34, s34, s46
	v_add_u32_e32 v0, s67, v0
	s_waitcnt lgkmcnt(0)
	s_add_u32 s6, s4, s38
	v_readfirstlane_b32 s4, v0
	s_addc_u32 s7, s5, s39
	v_and_b32_e32 v164, 31, v234
	v_or_b32_e32 v164, s67, v164
	v_ashrrev_i32_e32 v165, 31, v164
	v_lshl_add_u64 v[164:165], v[164:165], 2, s[6:7]
	global_load_dword v166, v[164:165], off
	global_load_dword v167, v[164:165], off offset:128
	s_ashr_i32 s10, s4, 7
	s_ashr_i32 s11, s10, 31
	s_and_b32 s5, s4, 64
	s_lshl_b64 s[10:11], s[10:11], 7
	v_and_b32_e32 v123, 31, v0
	s_or_b32 s5, s10, s5
	v_or_b32_e32 v2, s5, v123
	v_mov_b32_e32 v3, s11
	v_bfe_u32 v122, v0, 5, 1
	v_lshlrev_b64 v[2:3], 8, v[2:3]
	v_lshl_add_u64 v[2:3], s[8:9], 0, v[2:3]
	v_lshlrev_b32_e32 v0, 4, v122
	v_lshl_add_u64 v[6:7], v[2:3], 0, v[0:1]
	s_mov_b32 s5, 0x1600000
	v_add_co_u32_e32 v2, vcc, s5, v6
	s_mov_b64 s[8:9], 0x1600000
	s_nop 0
	v_addc_co_u32_e32 v3, vcc, 0, v7, vcc

	v_lshl_add_u64 v[114:115], v[6:7], 0, s[8:9]
	s_mov_b64 s[8:9], 0x1602000
	s_mov_b32 s5, 0x1602000
	v_lshl_add_u64 v[156:157], v[6:7], 0, s[8:9]
	v_add_co_u32_e32 v6, vcc, s5, v6
	s_lshl_b32 s5, s4, 1
	s_nop 0
	v_addc_co_u32_e32 v7, vcc, 0, v7, vcc

	s_nop 0


	s_and_b32 s5, s5, 0xffffff00
	v_mul_u32_u24_e32 v10, 0x410, v123
	v_or_b32_e32 v0, s5, v0
	v_add3_u32 v0, 0, v10, v0
	ds_read_b128 v[10:13], v0 offset:33280
	ds_read_b128 v[14:17], v0
	ds_read_b128 v[148:151], v0 offset:32
	ds_read_b128 v[152:155], v0 offset:33312
	s_andn2_b32 s4, s4, 63
	v_mul_u32_u24_e32 v122, 0x1040, v122
	s_cmpk_gt_i32 s34, 0x1ff
	s_waitcnt vmcnt(6) lgkmcnt(2)
	v_mfma_f32_32x32x16_bf16 v[18:33], v[14:17], v[172:175], 0
	v_mfma_f32_32x32x16_bf16 v[50:65], v[14:17], v[168:171], 0
	v_mfma_f32_32x32x16_bf16 v[34:49], v[10:13], v[168:171], 0
	v_mfma_f32_32x32x16_bf16 v[2:17], v[10:13], v[172:175], 0
	s_waitcnt vmcnt(5) lgkmcnt(1)
	v_mfma_f32_32x32x16_bf16 v[50:65], v[148:151], v[176:179], v[50:65]
	s_waitcnt vmcnt(4)
	v_mfma_f32_32x32x16_bf16 v[18:33], v[148:151], v[180:183], v[18:33]
	s_waitcnt lgkmcnt(0)
	v_mfma_f32_32x32x16_bf16 v[34:49], v[152:155], v[176:179], v[34:49]
	v_mfma_f32_32x32x16_bf16 v[2:17], v[152:155], v[180:183], v[2:17]
	ds_read_b128 v[124:127], v0 offset:64
	ds_read_b128 v[128:131], v0 offset:33344
	s_waitcnt vmcnt(3) lgkmcnt(1)
	v_mfma_f32_32x32x16_bf16 v[50:65], v[124:127], v[184:187], v[50:65]
	s_waitcnt vmcnt(2)
	v_mfma_f32_32x32x16_bf16 v[18:33], v[124:127], v[188:191], v[18:33]
	s_waitcnt lgkmcnt(0)
	v_mfma_f32_32x32x16_bf16 v[34:49], v[128:131], v[184:187], v[34:49]
	v_mfma_f32_32x32x16_bf16 v[2:17], v[128:131], v[188:191], v[2:17]
	ds_read_b128 v[124:127], v0 offset:96
	ds_read_b128 v[128:131], v0 offset:33376
	s_waitcnt vmcnt(1) lgkmcnt(1)
	v_mfma_f32_32x32x16_bf16 v[50:65], v[124:127], v[192:195], v[50:65]
	s_waitcnt vmcnt(0)
	v_mfma_f32_32x32x16_bf16 v[18:33], v[124:127], v[196:199], v[18:33]
	s_waitcnt lgkmcnt(0)
	v_mfma_f32_32x32x16_bf16 v[34:49], v[128:131], v[192:195], v[34:49]
	v_mfma_f32_32x32x16_bf16 v[2:17], v[128:131], v[196:199], v[2:17]


	ds_read_b128 v[156:159], v0 offset:128
	ds_read_b128 v[160:163], v0 offset:33408
	s_waitcnt vmcnt(7) lgkmcnt(1)
	v_mfma_f32_32x32x16_bf16 v[50:65], v[156:159], v[200:203], v[50:65]
	s_waitcnt vmcnt(6)
	v_mfma_f32_32x32x16_bf16 v[18:33], v[156:159], v[204:207], v[18:33]
	s_waitcnt lgkmcnt(0)
	v_mfma_f32_32x32x16_bf16 v[34:49], v[160:163], v[200:203], v[34:49]
	v_mfma_f32_32x32x16_bf16 v[2:17], v[160:163], v[204:207], v[2:17]
	ds_read_b128 v[124:127], v0 offset:160
	ds_read_b128 v[128:131], v0 offset:33440
	s_waitcnt vmcnt(5) lgkmcnt(1)
	v_mfma_f32_32x32x16_bf16 v[50:65], v[124:127], v[208:211], v[50:65]
	s_waitcnt vmcnt(4)
	v_mfma_f32_32x32x16_bf16 v[18:33], v[124:127], v[212:215], v[18:33]
	s_waitcnt lgkmcnt(0)
	v_mfma_f32_32x32x16_bf16 v[34:49], v[128:131], v[208:211], v[34:49]
	v_mfma_f32_32x32x16_bf16 v[2:17], v[128:131], v[212:215], v[2:17]
	ds_read_b128 v[124:127], v0 offset:192
	ds_read_b128 v[128:131], v0 offset:33472
	s_waitcnt vmcnt(3) lgkmcnt(1)
	v_mfma_f32_32x32x16_bf16 v[50:65], v[124:127], v[216:219], v[50:65]
	s_waitcnt vmcnt(2)
	v_mfma_f32_32x32x16_bf16 v[18:33], v[124:127], v[220:223], v[18:33]
	s_waitcnt lgkmcnt(0)
	v_mfma_f32_32x32x16_bf16 v[34:49], v[128:131], v[216:219], v[34:49]
	v_mfma_f32_32x32x16_bf16 v[2:17], v[128:131], v[220:223], v[2:17]
	ds_read_b128 v[124:127], v0 offset:224
	ds_read_b128 v[128:131], v0 offset:33504
	s_waitcnt lgkmcnt(0)
	s_barrier
	s_waitcnt vmcnt(1)
	v_mfma_f32_32x32x16_bf16 v[50:65], v[124:127], v[224:227], v[50:65]
	s_waitcnt vmcnt(0)
	v_mfma_f32_32x32x16_bf16 v[18:33], v[124:127], v[228:231], v[18:33]
	v_or_b32_e32 v124, s4, v123
	v_ashrrev_i32_e32 v125, 31, v124
	v_lshl_add_u64 v[114:115], v[124:125], 2, s[6:7]
	v_mov_b32_e32 v123, v166
	v_lshlrev_b32_e32 v0, 1, v124
	v_add3_u32 v0, 0, v0, v122
	s_waitcnt vmcnt(0)
	s_nop 2
	v_mul_f32_e32 v50, v50, v123
	v_mfma_f32_32x32x16_bf16 v[34:49], v[128:131], v[224:227], v[34:49]
	v_cvt_pk_bf16_f32 v50, v50, s0
	ds_write_b16 v0, v50
	v_mul_f32_e32 v50, v51, v123
	v_cvt_pk_bf16_f32 v50, v50, s0
	ds_write_b16 v0, v50 offset:1040
	v_mul_f32_e32 v50, v52, v123
	v_cvt_pk_bf16_f32 v50, v50, s0
	s_nop 4
	v_mul_f32_e32 v34, v34, v123
	v_cvt_pk_bf16_f32 v34, v34, s0
	ds_write_b16 v0, v34 offset:33280
	v_mul_f32_e32 v34, v35, v123
	v_cvt_pk_bf16_f32 v34, v34, s0
	ds_write_b16 v0, v34 offset:34320
	v_mul_f32_e32 v34, v36, v123
	v_cvt_pk_bf16_f32 v34, v34, s0
	ds_write_b16 v0, v34 offset:35360
	v_mul_f32_e32 v34, v37, v123
	v_cvt_pk_bf16_f32 v34, v34, s0
	ds_write_b16 v0, v34 offset:36400
	v_mul_f32_e32 v34, v38, v123
	v_cvt_pk_bf16_f32 v34, v34, s0
	ds_write_b16 v0, v34 offset:41600
	v_mul_f32_e32 v34, v39, v123
	v_cvt_pk_bf16_f32 v34, v34, s0
	ds_write_b16 v0, v34 offset:42640
	v_mul_f32_e32 v34, v40, v123
	v_cvt_pk_bf16_f32 v34, v34, s0
	ds_write_b16 v0, v34 offset:43680
	v_mul_f32_e32 v34, v41, v123
	v_cvt_pk_bf16_f32 v34, v34, s0
	ds_write_b16 v0, v34 offset:44720
	v_mul_f32_e32 v34, v42, v123
	v_cvt_pk_bf16_f32 v34, v34, s0
	ds_write_b16 v0, v34 offset:49920
	v_mul_f32_e32 v34, v43, v123
	v_cvt_pk_bf16_f32 v34, v34, s0
	ds_write_b16 v0, v34 offset:50960
	v_mul_f32_e32 v34, v44, v123
	v_cvt_pk_bf16_f32 v34, v34, s0
	ds_write_b16 v0, v34 offset:52000
	v_mul_f32_e32 v34, v45, v123
	v_cvt_pk_bf16_f32 v34, v34, s0
	ds_write_b16 v0, v34 offset:53040
	v_mul_f32_e32 v34, v46, v123
	v_cvt_pk_bf16_f32 v34, v34, s0
	ds_write_b16 v0, v34 offset:58240
	v_mul_f32_e32 v34, v47, v123
	v_cvt_pk_bf16_f32 v34, v34, s0
	ds_write_b16 v0, v34 offset:59280
	v_mul_f32_e32 v34, v48, v123
	v_cvt_pk_bf16_f32 v34, v34, s0
	ds_write_b16 v0, v34 offset:60320
	v_mul_f32_e32 v34, v49, v123
	v_cvt_pk_bf16_f32 v34, v34, s0
	ds_write_b16 v0, v34 offset:61360
	v_mov_b32_e32 v34, v167
	v_mfma_f32_32x32x16_bf16 v[2:17], v[128:131], v[228:231], v[2:17]
	ds_write_b16 v0, v50 offset:2080
	v_mul_f32_e32 v50, v53, v123
	v_cvt_pk_bf16_f32 v50, v50, s0
	ds_write_b16 v0, v50 offset:3120
	v_mul_f32_e32 v50, v54, v123
	v_cvt_pk_bf16_f32 v50, v50, s0
	ds_write_b16 v0, v50 offset:8320
	v_mul_f32_e32 v50, v55, v123
	v_cvt_pk_bf16_f32 v50, v50, s0
	ds_write_b16 v0, v50 offset:9360
	v_mul_f32_e32 v50, v56, v123
	v_cvt_pk_bf16_f32 v50, v50, s0
	ds_write_b16 v0, v50 offset:10400
	v_mul_f32_e32 v50, v57, v123
	v_cvt_pk_bf16_f32 v50, v50, s0
	ds_write_b16 v0, v50 offset:11440
	v_mul_f32_e32 v50, v58, v123
	v_cvt_pk_bf16_f32 v50, v50, s0
	ds_write_b16 v0, v50 offset:16640
	v_mul_f32_e32 v50, v59, v123
	v_cvt_pk_bf16_f32 v50, v50, s0
	ds_write_b16 v0, v50 offset:17680
	v_mul_f32_e32 v50, v60, v123
	v_cvt_pk_bf16_f32 v50, v50, s0
	ds_write_b16 v0, v50 offset:18720
	v_mul_f32_e32 v50, v61, v123
	v_cvt_pk_bf16_f32 v50, v50, s0
	ds_write_b16 v0, v50 offset:19760
	v_mul_f32_e32 v50, v62, v123
	v_cvt_pk_bf16_f32 v50, v50, s0
	ds_write_b16 v0, v50 offset:24960
	v_mul_f32_e32 v50, v63, v123
	v_cvt_pk_bf16_f32 v50, v50, s0
	ds_write_b16 v0, v50 offset:26000
	v_mul_f32_e32 v50, v64, v123
	v_cvt_pk_bf16_f32 v50, v50, s0
	ds_write_b16 v0, v50 offset:27040
	v_mul_f32_e32 v50, v65, v123
	v_cvt_pk_bf16_f32 v50, v50, s0
	ds_write_b16 v0, v50 offset:28080
	s_waitcnt vmcnt(0)
	v_mul_f32_e32 v18, v18, v34
	v_mul_f32_e32 v2, v2, v34
	v_cvt_pk_bf16_f32 v18, v18, s0
	v_cvt_pk_bf16_f32 v2, v2, s0
	ds_write_b16 v0, v18 offset:64
	v_mul_f32_e32 v18, v19, v34
	ds_write_b16 v0, v2 offset:33344
	v_mul_f32_e32 v2, v3, v34
	v_cvt_pk_bf16_f32 v18, v18, s0
	v_cvt_pk_bf16_f32 v2, v2, s0
	ds_write_b16 v0, v18 offset:1104
	v_mul_f32_e32 v18, v20, v34
	ds_write_b16 v0, v2 offset:34384
	v_mul_f32_e32 v2, v4, v34
	v_cvt_pk_bf16_f32 v18, v18, s0
	v_cvt_pk_bf16_f32 v2, v2, s0
	ds_write_b16 v0, v18 offset:2144
	v_mul_f32_e32 v18, v21, v34
	ds_write_b16 v0, v2 offset:35424
	v_mul_f32_e32 v2, v5, v34
	v_cvt_pk_bf16_f32 v18, v18, s0
	v_cvt_pk_bf16_f32 v2, v2, s0
	ds_write_b16 v0, v18 offset:3184
	v_mul_f32_e32 v18, v22, v34
	ds_write_b16 v0, v2 offset:36464
	v_mul_f32_e32 v2, v6, v34
	v_cvt_pk_bf16_f32 v18, v18, s0
	v_cvt_pk_bf16_f32 v2, v2, s0
	ds_write_b16 v0, v18 offset:8384
	v_mul_f32_e32 v18, v23, v34
	ds_write_b16 v0, v2 offset:41664
	v_mul_f32_e32 v2, v7, v34
	v_cvt_pk_bf16_f32 v18, v18, s0
	v_cvt_pk_bf16_f32 v2, v2, s0
	ds_write_b16 v0, v18 offset:9424
	v_mul_f32_e32 v18, v24, v34
	ds_write_b16 v0, v2 offset:42704
	v_mul_f32_e32 v2, v8, v34
	v_cvt_pk_bf16_f32 v18, v18, s0
	v_cvt_pk_bf16_f32 v2, v2, s0
	ds_write_b16 v0, v18 offset:10464
	v_mul_f32_e32 v18, v25, v34
	ds_write_b16 v0, v2 offset:43744
	v_mul_f32_e32 v2, v9, v34
	v_cvt_pk_bf16_f32 v18, v18, s0
	v_cvt_pk_bf16_f32 v2, v2, s0
	ds_write_b16 v0, v18 offset:11504
	v_mul_f32_e32 v18, v26, v34
	ds_write_b16 v0, v2 offset:44784
	v_mul_f32_e32 v2, v10, v34
	v_cvt_pk_bf16_f32 v18, v18, s0
	v_cvt_pk_bf16_f32 v2, v2, s0
	ds_write_b16 v0, v18 offset:16704
	v_mul_f32_e32 v18, v27, v34
	ds_write_b16 v0, v2 offset:49984
	v_mul_f32_e32 v2, v11, v34
	v_cvt_pk_bf16_f32 v18, v18, s0
	v_cvt_pk_bf16_f32 v2, v2, s0
	ds_write_b16 v0, v18 offset:17744
	v_mul_f32_e32 v18, v28, v34
	ds_write_b16 v0, v2 offset:51024
	v_mul_f32_e32 v2, v12, v34
	v_cvt_pk_bf16_f32 v18, v18, s0
	v_cvt_pk_bf16_f32 v2, v2, s0
	ds_write_b16 v0, v18 offset:18784
	v_mul_f32_e32 v18, v29, v34
	ds_write_b16 v0, v2 offset:52064
	v_mul_f32_e32 v2, v13, v34
	v_cvt_pk_bf16_f32 v18, v18, s0
	v_cvt_pk_bf16_f32 v2, v2, s0
	ds_write_b16 v0, v18 offset:19824
	v_mul_f32_e32 v18, v30, v34
	ds_write_b16 v0, v2 offset:53104
	v_mul_f32_e32 v2, v14, v34
	v_cvt_pk_bf16_f32 v18, v18, s0
	v_cvt_pk_bf16_f32 v2, v2, s0
	ds_write_b16 v0, v18 offset:25024
	v_mul_f32_e32 v18, v31, v34
	ds_write_b16 v0, v2 offset:58304
	v_mul_f32_e32 v2, v15, v34
	v_cvt_pk_bf16_f32 v18, v18, s0
	v_cvt_pk_bf16_f32 v2, v2, s0
	ds_write_b16 v0, v18 offset:26064
	v_mul_f32_e32 v18, v32, v34
	ds_write_b16 v0, v2 offset:59344
	v_mul_f32_e32 v2, v16, v34
	v_cvt_pk_bf16_f32 v18, v18, s0
	v_cvt_pk_bf16_f32 v2, v2, s0
	ds_write_b16 v0, v18 offset:27104
	v_mul_f32_e32 v18, v33, v34
	ds_write_b16 v0, v2 offset:60384
	v_mul_f32_e32 v2, v17, v34
	v_cvt_pk_bf16_f32 v18, v18, s0
	v_cvt_pk_bf16_f32 v2, v2, s0
	ds_write_b16 v0, v18 offset:28144
	ds_write_b16 v0, v2 offset:61424
	s_waitcnt lgkmcnt(0)
	s_barrier
	s_cbranch_scc1 .LBB0_599
	s_mov_b64 s[4:5], s[0:1]
	s_load_dwordx2 s[4:5], s[4:5], 0xd0
	s_bfe_i32 s9, s34, 0x10019
	v_mbcnt_lo_u32_b32 v0, -1, 0
	v_mbcnt_hi_u32_b32 v0, -1, v0
	s_lshl_b32 s8, s34, 6
	v_add_u32_e32 v8, s67, v0
	s_lshr_b32 s9, s9, 21
	s_add_i32 s9, s8, s9
	v_lshlrev_b32_e32 v0, 4, v8
	s_and_b32 s9, s9, 0xfffff800
	v_and_b32_e32 v0, 0x3f0, v0
	s_sub_i32 s8, s9, s8
	s_waitcnt lgkmcnt(0)
	v_lshl_add_u64 v[2:3], s[4:5], 0, v[0:1]
	v_min_i32_e32 v0, 0x177f, v8
	s_or_b32 s8, s8, 30
	v_ashrrev_i32_e32 v0, 6, v0
	s_ashr_i32 s35, s34, 31
	v_max_i32_e32 v4, s8, v0
	v_min_i32_e32 v0, 0x157f, v8
	s_lshl_b64 s[6:7], s[34:35], 6
	v_add_u32_e32 v0, 0x200, v0
	s_add_u32 s6, s6, 0xffffffe2
	v_ashrrev_i32_e32 v0, 6, v0
	s_addc_u32 s7, s7, -1
	v_ashrrev_i32_e32 v5, 31, v4
	v_max_i32_e32 v6, s8, v0
	s_mov_b64 s[4:5], 0xfc00000
	v_lshl_add_u64 v[4:5], s[6:7], 0, v[4:5]
	v_ashrrev_i32_e32 v7, 31, v6
	v_min_i32_e32 v0, 0x137f, v8
	v_lshl_add_u64 v[2:3], v[2:3], 0, s[4:5]
	v_lshlrev_b64 v[4:5], 10, v[4:5]
	v_lshl_add_u64 v[6:7], s[6:7], 0, v[6:7]
	v_add_u32_e32 v0, 0x400, v0
	v_lshl_add_u64 v[4:5], v[2:3], 0, v[4:5]
	v_lshlrev_b64 v[6:7], 10, v[6:7]
	v_ashrrev_i32_e32 v0, 6, v0
	v_lshl_add_u64 v[6:7], v[2:3], 0, v[6:7]
	global_load_dwordx4 v[66:69], v[4:5], off
	global_load_dwordx4 v[70:73], v[6:7], off
	v_max_i32_e32 v4, s8, v0
	v_min_i32_e32 v0, 0x117f, v8
	v_add_u32_e32 v0, 0x600, v0
	v_ashrrev_i32_e32 v0, 6, v0
	v_ashrrev_i32_e32 v5, 31, v4
	v_max_i32_e32 v6, s8, v0
	v_lshl_add_u64 v[4:5], s[6:7], 0, v[4:5]
	v_ashrrev_i32_e32 v7, 31, v6
	v_min_i32_e32 v0, 0xf7f, v8
	v_lshlrev_b64 v[4:5], 10, v[4:5]
	v_lshl_add_u64 v[6:7], s[6:7], 0, v[6:7]
	v_add_u32_e32 v0, 0x800, v0
	v_lshl_add_u64 v[4:5], v[2:3], 0, v[4:5]
	v_lshlrev_b64 v[6:7], 10, v[6:7]
	v_ashrrev_i32_e32 v0, 6, v0
	v_lshl_add_u64 v[6:7], v[2:3], 0, v[6:7]
	global_load_dwordx4 v[74:77], v[4:5], off
	global_load_dwordx4 v[78:81], v[6:7], off
	v_max_i32_e32 v4, s8, v0
	v_min_i32_e32 v0, 0xd7f, v8
	v_add_u32_e32 v0, 0xa00, v0
	v_ashrrev_i32_e32 v0, 6, v0
	v_ashrrev_i32_e32 v5, 31, v4
	v_max_i32_e32 v6, s8, v0
	v_lshl_add_u64 v[4:5], s[6:7], 0, v[4:5]
	v_ashrrev_i32_e32 v7, 31, v6
	v_min_i32_e32 v0, 0xb7f, v8
	v_lshlrev_b64 v[4:5], 10, v[4:5]
	v_lshl_add_u64 v[6:7], s[6:7], 0, v[6:7]
	v_add_u32_e32 v0, 0xc00, v0
	v_lshl_add_u64 v[4:5], v[2:3], 0, v[4:5]
	v_lshlrev_b64 v[6:7], 10, v[6:7]
	v_ashrrev_i32_e32 v0, 6, v0
	v_lshl_add_u64 v[6:7], v[2:3], 0, v[6:7]
	global_load_dwordx4 v[82:85], v[4:5], off
	global_load_dwordx4 v[86:89], v[6:7], off
	v_max_i32_e32 v4, s8, v0
	v_min_i32_e32 v0, 0x97f, v8
	v_add_u32_e32 v0, 0xe00, v0
	v_ashrrev_i32_e32 v0, 6, v0
	v_ashrrev_i32_e32 v5, 31, v4
	v_max_i32_e32 v6, s8, v0
	v_lshl_add_u64 v[4:5], s[6:7], 0, v[4:5]
	v_ashrrev_i32_e32 v7, 31, v6
	v_min_i32_e32 v0, 0x77f, v8
	v_lshlrev_b64 v[4:5], 10, v[4:5]
	v_lshl_add_u64 v[6:7], s[6:7], 0, v[6:7]
	v_add_u32_e32 v0, 0x1000, v0
	v_lshl_add_u64 v[4:5], v[2:3], 0, v[4:5]
	v_lshlrev_b64 v[6:7], 10, v[6:7]
	v_ashrrev_i32_e32 v0, 6, v0
	v_lshl_add_u64 v[6:7], v[2:3], 0, v[6:7]
	global_load_dwordx4 v[90:93], v[4:5], off
	global_load_dwordx4 v[94:97], v[6:7], off
	v_max_i32_e32 v4, s8, v0
	v_min_i32_e32 v0, 0x57f, v8
	v_add_u32_e32 v0, 0x1200, v0
	v_ashrrev_i32_e32 v0, 6, v0
	v_ashrrev_i32_e32 v5, 31, v4
	v_max_i32_e32 v6, s8, v0
	v_lshl_add_u64 v[4:5], s[6:7], 0, v[4:5]
	v_ashrrev_i32_e32 v7, 31, v6
	v_min_i32_e32 v0, 0x37f, v8
	v_lshlrev_b64 v[4:5], 10, v[4:5]
	v_lshl_add_u64 v[6:7], s[6:7], 0, v[6:7]
	v_add_u32_e32 v0, 0x1400, v0
	v_lshl_add_u64 v[4:5], v[2:3], 0, v[4:5]
	v_lshlrev_b64 v[6:7], 10, v[6:7]
	v_ashrrev_i32_e32 v0, 6, v0
	v_lshl_add_u64 v[6:7], v[2:3], 0, v[6:7]
	global_load_dwordx4 v[98:101], v[4:5], off
	global_load_dwordx4 v[102:105], v[6:7], off
	v_max_i32_e32 v4, s8, v0
	v_min_i32_e32 v0, 0x17f, v8
	v_add_u32_e32 v0, 0x1600, v0
	v_ashrrev_i32_e32 v0, 6, v0
	v_ashrrev_i32_e32 v5, 31, v4
	v_max_i32_e32 v6, s8, v0
	v_lshl_add_u64 v[4:5], s[6:7], 0, v[4:5]
	v_ashrrev_i32_e32 v7, 31, v6
	v_lshlrev_b64 v[4:5], 10, v[4:5]
	v_lshl_add_u64 v[6:7], s[6:7], 0, v[6:7]
	v_lshl_add_u64 v[4:5], v[2:3], 0, v[4:5]
	v_lshlrev_b64 v[6:7], 10, v[6:7]
	v_lshl_add_u64 v[2:3], v[2:3], 0, v[6:7]
	global_load_dwordx4 v[106:109], v[4:5], off
	global_load_dwordx4 v[110:113], v[2:3], off
